# speedup vs baseline: 1.0090x; 1.0041x over previous
.Lk2_b00:
	s_waitcnt lgkmcnt(4)
	v_mfma_f32_32x32x16_f16 v[16:31], v[144:147], v[80:83], v[16:31]
	s_cmp_le_u32 s22, 16
	s_cselect_b32 s40, s18, 0x18000
	s_add_u32 m0, s40, s35
	s_add_u32 s22, s22, 1
	global_load_lds_dwordx4 v168, s[20:21]
	global_load_lds_dwordx4 v168, s[20:21] offset:1024
	v_pk_mul_f16 v152, v48, v32 op_sel:[1,0] op_sel_hi:[1,1]
	v_pk_mul_f16 v153, v48, v33 op_sel:[1,0] op_sel_hi:[1,1]
	v_pk_mul_f16 v154, v48, v34 op_sel:[1,0] op_sel_hi:[1,1]
	v_pk_mul_f16 v155, v48, v35 op_sel:[1,0] op_sel_hi:[1,1]
	v_mfma_f32_32x32x16_f16 v[0:15], v[144:147], v[84:87], v[0:15]
	s_cmp_le_u32 s22, 16
	s_cselect_b32 s41, 0x4000, 0
	v_pk_fma_f16 v152, v40, v36, v152 op_sel:[1,0,0] op_sel_hi:[1,1,1]
	v_pk_fma_f16 v153, v40, v37, v153 op_sel:[1,0,0] op_sel_hi:[1,1,1]
	v_pk_fma_f16 v154, v40, v38, v154 op_sel:[1,0,0] op_sel_hi:[1,1,1]
	v_pk_fma_f16 v155, v40, v39, v155 op_sel:[1,0,0] op_sel_hi:[1,1,1]
	v_mfma_f32_32x32x16_f16 v[16:31], v[148:151], v[88:91], v[16:31]
	s_add_u32 s20, s20, s41
	s_addc_u32 s21, s21, 0
	v_pk_mul_f16 v156, v48, v36 op_sel:[1,0] op_sel_hi:[1,1]
	v_pk_mul_f16 v157, v48, v37 op_sel:[1,0] op_sel_hi:[1,1]
	v_pk_mul_f16 v158, v48, v38 op_sel:[1,0] op_sel_hi:[1,1]
	v_pk_mul_f16 v159, v48, v39 op_sel:[1,0] op_sel_hi:[1,1]
	v_mfma_f32_32x32x16_f16 v[0:15], v[148:151], v[92:95], v[0:15]
	s_add_u32 s18, s18, 0x4000
	s_cmp_eq_u32 s18, 0x18000
	s_cselect_b32 s18, 0, s18
	v_pk_fma_f16 v156, v40, v32, v156 op_sel:[1,0,0] op_sel_hi:[1,1,1] neg_lo:[0,0,1] neg_hi:[0,0,1]
	v_pk_fma_f16 v157, v40, v33, v157 op_sel:[1,0,0] op_sel_hi:[1,1,1] neg_lo:[0,0,1] neg_hi:[0,0,1]
	v_pk_fma_f16 v158, v40, v34, v158 op_sel:[1,0,0] op_sel_hi:[1,1,1] neg_lo:[0,0,1] neg_hi:[0,0,1]
	v_pk_fma_f16 v159, v40, v35, v159 op_sel:[1,0,0] op_sel_hi:[1,1,1] neg_lo:[0,0,1] neg_hi:[0,0,1]
	ds_read_b128 v[112:115], v161 offset:8192
	ds_read_b128 v[116:119], v161 offset:9216
	ds_read_b128 v[120:123], v161 offset:10240
	ds_read_b128 v[124:127], v161 offset:11264
	s_waitcnt lgkmcnt(4)
	v_mfma_f32_32x32x16_f16 v[16:31], v[152:155], v[96:99], v[16:31]
	s_add_u32 s14, s14, 1
	s_cmp_eq_u32 s14, 16
	s_cselect_b32 s42, 1, 0
	v_pk_mul_f16 v144, v49, v32 op_sel:[0,0] op_sel_hi:[0,1]
	v_pk_mul_f16 v145, v49, v33 op_sel:[0,0] op_sel_hi:[0,1]
	v_pk_mul_f16 v146, v49, v34 op_sel:[0,0] op_sel_hi:[0,1]
	v_pk_mul_f16 v147, v49, v35 op_sel:[0,0] op_sel_hi:[0,1]
	v_mfma_f32_32x32x16_f16 v[0:15], v[152:155], v[100:103], v[0:15]
	s_add_u32 s13, s13, s42
	s_cmp_eq_u32 s42, 1
	s_cselect_b32 s14, s13, s14
	v_pk_fma_f16 v144, v41, v36, v144 op_sel:[0,0,0] op_sel_hi:[0,1,1]
	v_pk_fma_f16 v145, v41, v37, v145 op_sel:[0,0,0] op_sel_hi:[0,1,1]
	v_pk_fma_f16 v146, v41, v38, v146 op_sel:[0,0,0] op_sel_hi:[0,1,1]
	v_pk_fma_f16 v147, v41, v39, v147 op_sel:[0,0,0] op_sel_hi:[0,1,1]
	v_mfma_f32_32x32x16_f16 v[16:31], v[156:159], v[104:107], v[16:31]
	s_min_u32 s43, s13, 15
	s_min_u32 s44, s14, 15
	s_lshl_b32 s45, s44, 16
	v_pk_mul_f16 v148, v49, v36 op_sel:[0,0] op_sel_hi:[0,1]
	v_pk_mul_f16 v149, v49, v37 op_sel:[0,0] op_sel_hi:[0,1]
	v_pk_mul_f16 v150, v49, v38 op_sel:[0,0] op_sel_hi:[0,1]
	v_pk_mul_f16 v151, v49, v39 op_sel:[0,0] op_sel_hi:[0,1]
	v_mfma_f32_32x32x16_f16 v[0:15], v[156:159], v[108:111], v[0:15]
	s_add_u32 s24, s8, s45
	s_addc_u32 s25, s9, 0
	v_pk_fma_f16 v148, v41, v32, v148 op_sel:[0,0,0] op_sel_hi:[0,1,1] neg_lo:[0,0,1] neg_hi:[0,0,1]
	v_pk_fma_f16 v149, v41, v33, v149 op_sel:[0,0,0] op_sel_hi:[0,1,1] neg_lo:[0,0,1] neg_hi:[0,0,1]
	v_pk_fma_f16 v150, v41, v34, v150 op_sel:[0,0,0] op_sel_hi:[0,1,1] neg_lo:[0,0,1] neg_hi:[0,0,1]
	v_pk_fma_f16 v151, v41, v35, v151 op_sel:[0,0,0] op_sel_hi:[0,1,1] neg_lo:[0,0,1] neg_hi:[0,0,1]
	ds_read_b128 v[128:131], v161 offset:12288
	ds_read_b128 v[132:135], v161 offset:13312
	ds_read_b128 v[136:139], v161 offset:14336
	ds_read_b128 v[140:143], v161 offset:15360
	s_add_u32 s19, s19, 0x4000
	s_cmp_eq_u32 s19, 0x18000
	s_cselect_b32 s19, 0, s19
	v_add_u32_e32 v161, s19, v160
	s_waitcnt lgkmcnt(4)
	v_mfma_f32_32x32x16_f16 v[16:31], v[144:147], v[112:115], v[16:31]
	s_add_u32 s26, s24, 0x100000
	s_addc_u32 s27, s25, 0
	s_lshl_b32 s45, s43, 16
	s_add_u32 s28, s8, s45
	s_addc_u32 s29, s9, 0
	v_pk_mul_f16 v152, v49, v32 op_sel:[1,0] op_sel_hi:[1,1]
	v_pk_mul_f16 v153, v49, v33 op_sel:[1,0] op_sel_hi:[1,1]
	v_pk_mul_f16 v154, v49, v34 op_sel:[1,0] op_sel_hi:[1,1]
	v_pk_mul_f16 v155, v49, v35 op_sel:[1,0] op_sel_hi:[1,1]
	v_mfma_f32_32x32x16_f16 v[0:15], v[144:147], v[116:119], v[0:15]
	s_add_u32 s30, s28, 0x100000
	s_addc_u32 s31, s29, 0
	v_pk_fma_f16 v152, v41, v36, v152 op_sel:[1,0,0] op_sel_hi:[1,1,1]
	v_pk_fma_f16 v153, v41, v37, v153 op_sel:[1,0,0] op_sel_hi:[1,1,1]
	v_pk_fma_f16 v154, v41, v38, v154 op_sel:[1,0,0] op_sel_hi:[1,1,1]
	v_pk_fma_f16 v155, v41, v39, v155 op_sel:[1,0,0] op_sel_hi:[1,1,1]
	v_mfma_f32_32x32x16_f16 v[16:31], v[148:151], v[120:123], v[16:31]
	global_load_dwordx4 v[60:63], v164, s[24:25]
	v_pk_mul_f16 v156, v49, v36 op_sel:[1,0] op_sel_hi:[1,1]
	v_pk_mul_f16 v157, v49, v37 op_sel:[1,0] op_sel_hi:[1,1]
	v_pk_mul_f16 v158, v49, v38 op_sel:[1,0] op_sel_hi:[1,1]
	v_pk_mul_f16 v159, v49, v39 op_sel:[1,0] op_sel_hi:[1,1]
	v_mfma_f32_32x32x16_f16 v[0:15], v[148:151], v[124:127], v[0:15]
	global_load_dwordx4 v[56:59], v164, s[26:27]
	v_pk_fma_f16 v156, v41, v32, v156 op_sel:[1,0,0] op_sel_hi:[1,1,1] neg_lo:[0,0,1] neg_hi:[0,0,1]
	v_pk_fma_f16 v157, v41, v33, v157 op_sel:[1,0,0] op_sel_hi:[1,1,1] neg_lo:[0,0,1] neg_hi:[0,0,1]
	v_pk_fma_f16 v158, v41, v34, v158 op_sel:[1,0,0] op_sel_hi:[1,1,1] neg_lo:[0,0,1] neg_hi:[0,0,1]
	v_pk_fma_f16 v159, v41, v35, v159 op_sel:[1,0,0] op_sel_hi:[1,1,1] neg_lo:[0,0,1] neg_hi:[0,0,1]
	ds_read_b128 v[80:83], v161
	ds_read_b128 v[84:87], v161 offset:1024
	ds_read_b128 v[88:91], v161 offset:2048
	ds_read_b128 v[92:95], v161 offset:3072
	s_waitcnt lgkmcnt(4)
	v_mfma_f32_32x32x16_f16 v[16:31], v[152:155], v[128:131], v[16:31]
	global_load_dwordx4 v[64:67], v165, s[28:29]
	v_pk_mul_f16 v144, v50, v32 op_sel:[0,0] op_sel_hi:[0,1]
	v_pk_mul_f16 v145, v50, v33 op_sel:[0,0] op_sel_hi:[0,1]
	v_pk_mul_f16 v146, v50, v34 op_sel:[0,0] op_sel_hi:[0,1]
	v_pk_mul_f16 v147, v50, v35 op_sel:[0,0] op_sel_hi:[0,1]
	v_mfma_f32_32x32x16_f16 v[0:15], v[152:155], v[132:135], v[0:15]
	global_load_dwordx4 v[68:71], v166, s[28:29]
	v_pk_fma_f16 v144, v42, v36, v144 op_sel:[0,0,0] op_sel_hi:[0,1,1]
	v_pk_fma_f16 v145, v42, v37, v145 op_sel:[0,0,0] op_sel_hi:[0,1,1]
	v_pk_fma_f16 v146, v42, v38, v146 op_sel:[0,0,0] op_sel_hi:[0,1,1]
	v_pk_fma_f16 v147, v42, v39, v147 op_sel:[0,0,0] op_sel_hi:[0,1,1]
	v_mfma_f32_32x32x16_f16 v[16:31], v[156:159], v[136:139], v[16:31]
	global_load_dwordx4 v[72:75], v165, s[30:31]
	v_pk_mul_f16 v148, v50, v36 op_sel:[0,0] op_sel_hi:[0,1]
	v_pk_mul_f16 v149, v50, v37 op_sel:[0,0] op_sel_hi:[0,1]
	v_pk_mul_f16 v150, v50, v38 op_sel:[0,0] op_sel_hi:[0,1]
	v_pk_mul_f16 v151, v50, v39 op_sel:[0,0] op_sel_hi:[0,1]
	v_mfma_f32_32x32x16_f16 v[0:15], v[156:159], v[140:143], v[0:15]
	global_load_dwordx4 v[76:79], v166, s[30:31]
	v_pk_fma_f16 v148, v42, v32, v148 op_sel:[0,0,0] op_sel_hi:[0,1,1] neg_lo:[0,0,1] neg_hi:[0,0,1]
	v_pk_fma_f16 v149, v42, v33, v149 op_sel:[0,0,0] op_sel_hi:[0,1,1] neg_lo:[0,0,1] neg_hi:[0,0,1]
	v_pk_fma_f16 v150, v42, v34, v150 op_sel:[0,0,0] op_sel_hi:[0,1,1] neg_lo:[0,0,1] neg_hi:[0,0,1]
	v_pk_fma_f16 v151, v42, v35, v151 op_sel:[0,0,0] op_sel_hi:[0,1,1] neg_lo:[0,0,1] neg_hi:[0,0,1]
	ds_read_b128 v[96:99], v161 offset:4096
	ds_read_b128 v[100:103], v161 offset:5120
	ds_read_b128 v[104:107], v161 offset:6144
	ds_read_b128 v[108:111], v161 offset:7168
	s_add_u32 s17, s17, 1
	s_cmp_eq_u32 s17, 17
	s_cbranch_scc1 .Lk2_epi

.Lk2_b01:
	s_waitcnt lgkmcnt(4)
	v_mfma_f32_32x32x16_f16 v[16:31], v[144:147], v[80:83], v[16:31]
	s_cmp_le_u32 s22, 16
	s_cselect_b32 s40, s18, 0x18000
	s_add_u32 m0, s40, s35
	v_pk_mul_f16 v152, v50, v32 op_sel:[1,0] op_sel_hi:[1,1]
	v_pk_mul_f16 v153, v50, v33 op_sel:[1,0] op_sel_hi:[1,1]
	v_pk_mul_f16 v154, v50, v34 op_sel:[1,0] op_sel_hi:[1,1]
	v_pk_mul_f16 v155, v50, v35 op_sel:[1,0] op_sel_hi:[1,1]
	v_mfma_f32_32x32x16_f16 v[0:15], v[144:147], v[84:87], v[0:15]
	s_add_u32 s22, s22, 1
	global_load_lds_dwordx4 v168, s[20:21]
	global_load_lds_dwordx4 v168, s[20:21] offset:1024
	v_pk_fma_f16 v152, v42, v36, v152 op_sel:[1,0,0] op_sel_hi:[1,1,1]
	v_pk_fma_f16 v153, v42, v37, v153 op_sel:[1,0,0] op_sel_hi:[1,1,1]
	v_pk_fma_f16 v154, v42, v38, v154 op_sel:[1,0,0] op_sel_hi:[1,1,1]
	v_pk_fma_f16 v155, v42, v39, v155 op_sel:[1,0,0] op_sel_hi:[1,1,1]
	v_mfma_f32_32x32x16_f16 v[16:31], v[148:151], v[88:91], v[16:31]
	s_cmp_le_u32 s22, 16
	s_cselect_b32 s41, 0x4000, 0
	v_pk_mul_f16 v156, v50, v36 op_sel:[1,0] op_sel_hi:[1,1]
	v_pk_mul_f16 v157, v50, v37 op_sel:[1,0] op_sel_hi:[1,1]
	v_pk_mul_f16 v158, v50, v38 op_sel:[1,0] op_sel_hi:[1,1]
	v_pk_mul_f16 v159, v50, v39 op_sel:[1,0] op_sel_hi:[1,1]
	v_mfma_f32_32x32x16_f16 v[0:15], v[148:151], v[92:95], v[0:15]
	s_add_u32 s20, s20, s41
	s_addc_u32 s21, s21, 0
	v_pk_fma_f16 v156, v42, v32, v156 op_sel:[1,0,0] op_sel_hi:[1,1,1] neg_lo:[0,0,1] neg_hi:[0,0,1]
	v_pk_fma_f16 v157, v42, v33, v157 op_sel:[1,0,0] op_sel_hi:[1,1,1] neg_lo:[0,0,1] neg_hi:[0,0,1]
	v_pk_fma_f16 v158, v42, v34, v158 op_sel:[1,0,0] op_sel_hi:[1,1,1] neg_lo:[0,0,1] neg_hi:[0,0,1]
	v_pk_fma_f16 v159, v42, v35, v159 op_sel:[1,0,0] op_sel_hi:[1,1,1] neg_lo:[0,0,1] neg_hi:[0,0,1]
	ds_read_b128 v[112:115], v161 offset:8192
	ds_read_b128 v[116:119], v161 offset:9216
	ds_read_b128 v[120:123], v161 offset:10240
	ds_read_b128 v[124:127], v161 offset:11264
	s_waitcnt lgkmcnt(4)
	v_mfma_f32_32x32x16_f16 v[16:31], v[152:155], v[96:99], v[16:31]
	s_add_u32 s18, s18, 0x4000
	s_cmp_eq_u32 s18, 0x18000
	s_cselect_b32 s18, 0, s18
	v_pk_mul_f16 v144, v51, v32 op_sel:[0,0] op_sel_hi:[0,1]
	v_pk_mul_f16 v145, v51, v33 op_sel:[0,0] op_sel_hi:[0,1]
	v_pk_mul_f16 v146, v51, v34 op_sel:[0,0] op_sel_hi:[0,1]
	v_pk_mul_f16 v147, v51, v35 op_sel:[0,0] op_sel_hi:[0,1]
	v_mfma_f32_32x32x16_f16 v[0:15], v[152:155], v[100:103], v[0:15]
	v_pk_fma_f16 v144, v43, v36, v144 op_sel:[0,0,0] op_sel_hi:[0,1,1]
	v_pk_fma_f16 v145, v43, v37, v145 op_sel:[0,0,0] op_sel_hi:[0,1,1]
	v_pk_fma_f16 v146, v43, v38, v146 op_sel:[0,0,0] op_sel_hi:[0,1,1]
	v_pk_fma_f16 v147, v43, v39, v147 op_sel:[0,0,0] op_sel_hi:[0,1,1]
	v_mfma_f32_32x32x16_f16 v[16:31], v[156:159], v[104:107], v[16:31]
	v_pk_mul_f16 v148, v51, v36 op_sel:[0,0] op_sel_hi:[0,1]
	v_pk_mul_f16 v149, v51, v37 op_sel:[0,0] op_sel_hi:[0,1]
	v_pk_mul_f16 v150, v51, v38 op_sel:[0,0] op_sel_hi:[0,1]
	v_pk_mul_f16 v151, v51, v39 op_sel:[0,0] op_sel_hi:[0,1]
	v_mfma_f32_32x32x16_f16 v[0:15], v[156:159], v[108:111], v[0:15]
	v_pk_fma_f16 v148, v43, v32, v148 op_sel:[0,0,0] op_sel_hi:[0,1,1] neg_lo:[0,0,1] neg_hi:[0,0,1]
	v_pk_fma_f16 v149, v43, v33, v149 op_sel:[0,0,0] op_sel_hi:[0,1,1] neg_lo:[0,0,1] neg_hi:[0,0,1]
	v_pk_fma_f16 v150, v43, v34, v150 op_sel:[0,0,0] op_sel_hi:[0,1,1] neg_lo:[0,0,1] neg_hi:[0,0,1]
	v_pk_fma_f16 v151, v43, v35, v151 op_sel:[0,0,0] op_sel_hi:[0,1,1] neg_lo:[0,0,1] neg_hi:[0,0,1]
	ds_read_b128 v[128:131], v161 offset:12288
	ds_read_b128 v[132:135], v161 offset:13312
	ds_read_b128 v[136:139], v161 offset:14336
	ds_read_b128 v[140:143], v161 offset:15360
	s_add_u32 s19, s19, 0x4000
	s_cmp_eq_u32 s19, 0x18000
	s_cselect_b32 s19, 0, s19
	v_add_u32_e32 v161, s19, v160
	s_waitcnt lgkmcnt(4)
	v_mfma_f32_32x32x16_f16 v[16:31], v[144:147], v[112:115], v[16:31]
	v_pk_mul_f16 v152, v51, v32 op_sel:[1,0] op_sel_hi:[1,1]
	v_pk_mul_f16 v153, v51, v33 op_sel:[1,0] op_sel_hi:[1,1]
	v_pk_mul_f16 v154, v51, v34 op_sel:[1,0] op_sel_hi:[1,1]
	v_pk_mul_f16 v155, v51, v35 op_sel:[1,0] op_sel_hi:[1,1]
	v_mfma_f32_32x32x16_f16 v[0:15], v[144:147], v[116:119], v[0:15]
	v_pk_fma_f16 v152, v43, v36, v152 op_sel:[1,0,0] op_sel_hi:[1,1,1]
	v_pk_fma_f16 v153, v43, v37, v153 op_sel:[1,0,0] op_sel_hi:[1,1,1]
	v_pk_fma_f16 v154, v43, v38, v154 op_sel:[1,0,0] op_sel_hi:[1,1,1]
	v_pk_fma_f16 v155, v43, v39, v155 op_sel:[1,0,0] op_sel_hi:[1,1,1]
	v_mfma_f32_32x32x16_f16 v[16:31], v[148:151], v[120:123], v[16:31]
	v_pk_mul_f16 v156, v51, v36 op_sel:[1,0] op_sel_hi:[1,1]
	v_pk_mul_f16 v157, v51, v37 op_sel:[1,0] op_sel_hi:[1,1]
	v_pk_mul_f16 v158, v51, v38 op_sel:[1,0] op_sel_hi:[1,1]
	v_pk_mul_f16 v159, v51, v39 op_sel:[1,0] op_sel_hi:[1,1]
	v_mfma_f32_32x32x16_f16 v[0:15], v[148:151], v[124:127], v[0:15]
	v_pk_fma_f16 v156, v43, v32, v156 op_sel:[1,0,0] op_sel_hi:[1,1,1] neg_lo:[0,0,1] neg_hi:[0,0,1]
	v_pk_fma_f16 v157, v43, v33, v157 op_sel:[1,0,0] op_sel_hi:[1,1,1] neg_lo:[0,0,1] neg_hi:[0,0,1]
	v_pk_fma_f16 v158, v43, v34, v158 op_sel:[1,0,0] op_sel_hi:[1,1,1] neg_lo:[0,0,1] neg_hi:[0,0,1]
	v_pk_fma_f16 v159, v43, v35, v159 op_sel:[1,0,0] op_sel_hi:[1,1,1] neg_lo:[0,0,1] neg_hi:[0,0,1]
	ds_read_b128 v[80:83], v161
	ds_read_b128 v[84:87], v161 offset:1024
	ds_read_b128 v[88:91], v161 offset:2048
	ds_read_b128 v[92:95], v161 offset:3072
	s_waitcnt lgkmcnt(4)
	v_mfma_f32_32x32x16_f16 v[16:31], v[152:155], v[128:131], v[16:31]
	v_pk_mul_f16 v144, v52, v32 op_sel:[0,0] op_sel_hi:[0,1]
	v_pk_mul_f16 v145, v52, v33 op_sel:[0,0] op_sel_hi:[0,1]
	v_pk_mul_f16 v146, v52, v34 op_sel:[0,0] op_sel_hi:[0,1]
	v_pk_mul_f16 v147, v52, v35 op_sel:[0,0] op_sel_hi:[0,1]
	v_mfma_f32_32x32x16_f16 v[0:15], v[152:155], v[132:135], v[0:15]
	v_pk_fma_f16 v144, v44, v36, v144 op_sel:[0,0,0] op_sel_hi:[0,1,1]
	v_pk_fma_f16 v145, v44, v37, v145 op_sel:[0,0,0] op_sel_hi:[0,1,1]
	v_pk_fma_f16 v146, v44, v38, v146 op_sel:[0,0,0] op_sel_hi:[0,1,1]
	v_pk_fma_f16 v147, v44, v39, v147 op_sel:[0,0,0] op_sel_hi:[0,1,1]
	v_mfma_f32_32x32x16_f16 v[16:31], v[156:159], v[136:139], v[16:31]
	v_pk_mul_f16 v148, v52, v36 op_sel:[0,0] op_sel_hi:[0,1]
	v_pk_mul_f16 v149, v52, v37 op_sel:[0,0] op_sel_hi:[0,1]
	v_pk_mul_f16 v150, v52, v38 op_sel:[0,0] op_sel_hi:[0,1]
	v_pk_mul_f16 v151, v52, v39 op_sel:[0,0] op_sel_hi:[0,1]
	v_mfma_f32_32x32x16_f16 v[0:15], v[156:159], v[140:143], v[0:15]
	v_pk_fma_f16 v148, v44, v32, v148 op_sel:[0,0,0] op_sel_hi:[0,1,1] neg_lo:[0,0,1] neg_hi:[0,0,1]
	v_pk_fma_f16 v149, v44, v33, v149 op_sel:[0,0,0] op_sel_hi:[0,1,1] neg_lo:[0,0,1] neg_hi:[0,0,1]
	v_pk_fma_f16 v150, v44, v34, v150 op_sel:[0,0,0] op_sel_hi:[0,1,1] neg_lo:[0,0,1] neg_hi:[0,0,1]
	v_pk_fma_f16 v151, v44, v35, v151 op_sel:[0,0,0] op_sel_hi:[0,1,1] neg_lo:[0,0,1] neg_hi:[0,0,1]
	ds_read_b128 v[96:99], v161 offset:4096
	ds_read_b128 v[100:103], v161 offset:5120
	ds_read_b128 v[104:107], v161 offset:6144
	ds_read_b128 v[108:111], v161 offset:7168
	s_add_u32 s17, s17, 1
	s_cmp_eq_u32 s17, 17
	s_cbranch_scc1 .Lk2_epi

.Lk2_b02:
	s_waitcnt lgkmcnt(4)
	v_mfma_f32_32x32x16_f16 v[16:31], v[144:147], v[80:83], v[16:31]
	s_cmp_le_u32 s22, 16
	s_cselect_b32 s40, s18, 0x18000
	s_add_u32 m0, s40, s35
	v_pk_mul_f16 v152, v52, v32 op_sel:[1,0] op_sel_hi:[1,1]
	v_pk_mul_f16 v153, v52, v33 op_sel:[1,0] op_sel_hi:[1,1]
	v_pk_mul_f16 v154, v52, v34 op_sel:[1,0] op_sel_hi:[1,1]
	v_pk_mul_f16 v155, v52, v35 op_sel:[1,0] op_sel_hi:[1,1]
	v_mfma_f32_32x32x16_f16 v[0:15], v[144:147], v[84:87], v[0:15]
	s_add_u32 s22, s22, 1
	global_load_lds_dwordx4 v168, s[20:21]
	global_load_lds_dwordx4 v168, s[20:21] offset:1024
	v_pk_fma_f16 v152, v44, v36, v152 op_sel:[1,0,0] op_sel_hi:[1,1,1]
	v_pk_fma_f16 v153, v44, v37, v153 op_sel:[1,0,0] op_sel_hi:[1,1,1]
	v_pk_fma_f16 v154, v44, v38, v154 op_sel:[1,0,0] op_sel_hi:[1,1,1]
	v_pk_fma_f16 v155, v44, v39, v155 op_sel:[1,0,0] op_sel_hi:[1,1,1]
	v_mfma_f32_32x32x16_f16 v[16:31], v[148:151], v[88:91], v[16:31]
	s_cmp_le_u32 s22, 16
	s_cselect_b32 s41, 0x4000, 0
	v_pk_mul_f16 v156, v52, v36 op_sel:[1,0] op_sel_hi:[1,1]
	v_pk_mul_f16 v157, v52, v37 op_sel:[1,0] op_sel_hi:[1,1]
	v_pk_mul_f16 v158, v52, v38 op_sel:[1,0] op_sel_hi:[1,1]
	v_pk_mul_f16 v159, v52, v39 op_sel:[1,0] op_sel_hi:[1,1]
	v_mfma_f32_32x32x16_f16 v[0:15], v[148:151], v[92:95], v[0:15]
	s_add_u32 s20, s20, s41
	s_addc_u32 s21, s21, 0
	v_pk_fma_f16 v156, v44, v32, v156 op_sel:[1,0,0] op_sel_hi:[1,1,1] neg_lo:[0,0,1] neg_hi:[0,0,1]
	v_pk_fma_f16 v157, v44, v33, v157 op_sel:[1,0,0] op_sel_hi:[1,1,1] neg_lo:[0,0,1] neg_hi:[0,0,1]
	v_pk_fma_f16 v158, v44, v34, v158 op_sel:[1,0,0] op_sel_hi:[1,1,1] neg_lo:[0,0,1] neg_hi:[0,0,1]
	v_pk_fma_f16 v159, v44, v35, v159 op_sel:[1,0,0] op_sel_hi:[1,1,1] neg_lo:[0,0,1] neg_hi:[0,0,1]
	ds_read_b128 v[112:115], v161 offset:8192
	ds_read_b128 v[116:119], v161 offset:9216
	ds_read_b128 v[120:123], v161 offset:10240
	ds_read_b128 v[124:127], v161 offset:11264
	s_waitcnt lgkmcnt(4)
	v_mfma_f32_32x32x16_f16 v[16:31], v[152:155], v[96:99], v[16:31]
	s_add_u32 s18, s18, 0x4000
	s_cmp_eq_u32 s18, 0x18000
	s_cselect_b32 s18, 0, s18
	v_pk_mul_f16 v144, v53, v32 op_sel:[0,0] op_sel_hi:[0,1]
	v_pk_mul_f16 v145, v53, v33 op_sel:[0,0] op_sel_hi:[0,1]
	v_pk_mul_f16 v146, v53, v34 op_sel:[0,0] op_sel_hi:[0,1]
	v_pk_mul_f16 v147, v53, v35 op_sel:[0,0] op_sel_hi:[0,1]
	v_mfma_f32_32x32x16_f16 v[0:15], v[152:155], v[100:103], v[0:15]
	v_pk_fma_f16 v144, v45, v36, v144 op_sel:[0,0,0] op_sel_hi:[0,1,1]
	v_pk_fma_f16 v145, v45, v37, v145 op_sel:[0,0,0] op_sel_hi:[0,1,1]
	v_pk_fma_f16 v146, v45, v38, v146 op_sel:[0,0,0] op_sel_hi:[0,1,1]
	v_pk_fma_f16 v147, v45, v39, v147 op_sel:[0,0,0] op_sel_hi:[0,1,1]
	v_mfma_f32_32x32x16_f16 v[16:31], v[156:159], v[104:107], v[16:31]
	v_pk_mul_f16 v148, v53, v36 op_sel:[0,0] op_sel_hi:[0,1]
	v_pk_mul_f16 v149, v53, v37 op_sel:[0,0] op_sel_hi:[0,1]
	v_pk_mul_f16 v150, v53, v38 op_sel:[0,0] op_sel_hi:[0,1]
	v_pk_mul_f16 v151, v53, v39 op_sel:[0,0] op_sel_hi:[0,1]
	v_mfma_f32_32x32x16_f16 v[0:15], v[156:159], v[108:111], v[0:15]
	v_pk_fma_f16 v148, v45, v32, v148 op_sel:[0,0,0] op_sel_hi:[0,1,1] neg_lo:[0,0,1] neg_hi:[0,0,1]
	v_pk_fma_f16 v149, v45, v33, v149 op_sel:[0,0,0] op_sel_hi:[0,1,1] neg_lo:[0,0,1] neg_hi:[0,0,1]
	v_pk_fma_f16 v150, v45, v34, v150 op_sel:[0,0,0] op_sel_hi:[0,1,1] neg_lo:[0,0,1] neg_hi:[0,0,1]
	v_pk_fma_f16 v151, v45, v35, v151 op_sel:[0,0,0] op_sel_hi:[0,1,1] neg_lo:[0,0,1] neg_hi:[0,0,1]
	ds_read_b128 v[128:131], v161 offset:12288
	ds_read_b128 v[132:135], v161 offset:13312
	ds_read_b128 v[136:139], v161 offset:14336
	ds_read_b128 v[140:143], v161 offset:15360
	s_add_u32 s19, s19, 0x4000
	s_cmp_eq_u32 s19, 0x18000
	s_cselect_b32 s19, 0, s19
	v_add_u32_e32 v161, s19, v160
	s_waitcnt lgkmcnt(4)
	v_mfma_f32_32x32x16_f16 v[16:31], v[144:147], v[112:115], v[16:31]
	v_pk_mul_f16 v152, v53, v32 op_sel:[1,0] op_sel_hi:[1,1]
	v_pk_mul_f16 v153, v53, v33 op_sel:[1,0] op_sel_hi:[1,1]
	v_pk_mul_f16 v154, v53, v34 op_sel:[1,0] op_sel_hi:[1,1]
	v_pk_mul_f16 v155, v53, v35 op_sel:[1,0] op_sel_hi:[1,1]
	v_mfma_f32_32x32x16_f16 v[0:15], v[144:147], v[116:119], v[0:15]
	v_pk_fma_f16 v152, v45, v36, v152 op_sel:[1,0,0] op_sel_hi:[1,1,1]
	v_pk_fma_f16 v153, v45, v37, v153 op_sel:[1,0,0] op_sel_hi:[1,1,1]
	v_pk_fma_f16 v154, v45, v38, v154 op_sel:[1,0,0] op_sel_hi:[1,1,1]
	v_pk_fma_f16 v155, v45, v39, v155 op_sel:[1,0,0] op_sel_hi:[1,1,1]
	v_mfma_f32_32x32x16_f16 v[16:31], v[148:151], v[120:123], v[16:31]
	v_pk_mul_f16 v156, v53, v36 op_sel:[1,0] op_sel_hi:[1,1]
	v_pk_mul_f16 v157, v53, v37 op_sel:[1,0] op_sel_hi:[1,1]
	v_pk_mul_f16 v158, v53, v38 op_sel:[1,0] op_sel_hi:[1,1]
	v_pk_mul_f16 v159, v53, v39 op_sel:[1,0] op_sel_hi:[1,1]
	v_mfma_f32_32x32x16_f16 v[0:15], v[148:151], v[124:127], v[0:15]
	v_pk_fma_f16 v156, v45, v32, v156 op_sel:[1,0,0] op_sel_hi:[1,1,1] neg_lo:[0,0,1] neg_hi:[0,0,1]
	v_pk_fma_f16 v157, v45, v33, v157 op_sel:[1,0,0] op_sel_hi:[1,1,1] neg_lo:[0,0,1] neg_hi:[0,0,1]
	v_pk_fma_f16 v158, v45, v34, v158 op_sel:[1,0,0] op_sel_hi:[1,1,1] neg_lo:[0,0,1] neg_hi:[0,0,1]
	v_pk_fma_f16 v159, v45, v35, v159 op_sel:[1,0,0] op_sel_hi:[1,1,1] neg_lo:[0,0,1] neg_hi:[0,0,1]
	ds_read_b128 v[80:83], v161
	ds_read_b128 v[84:87], v161 offset:1024
	ds_read_b128 v[88:91], v161 offset:2048
	ds_read_b128 v[92:95], v161 offset:3072
	s_waitcnt lgkmcnt(4)
	v_mfma_f32_32x32x16_f16 v[16:31], v[152:155], v[128:131], v[16:31]
	v_pk_mul_f16 v144, v54, v32 op_sel:[0,0] op_sel_hi:[0,1]
	v_pk_mul_f16 v145, v54, v33 op_sel:[0,0] op_sel_hi:[0,1]
	v_pk_mul_f16 v146, v54, v34 op_sel:[0,0] op_sel_hi:[0,1]
	v_pk_mul_f16 v147, v54, v35 op_sel:[0,0] op_sel_hi:[0,1]
	v_mfma_f32_32x32x16_f16 v[0:15], v[152:155], v[132:135], v[0:15]
	v_pk_fma_f16 v144, v46, v36, v144 op_sel:[0,0,0] op_sel_hi:[0,1,1]
	v_pk_fma_f16 v145, v46, v37, v145 op_sel:[0,0,0] op_sel_hi:[0,1,1]
	v_pk_fma_f16 v146, v46, v38, v146 op_sel:[0,0,0] op_sel_hi:[0,1,1]
	v_pk_fma_f16 v147, v46, v39, v147 op_sel:[0,0,0] op_sel_hi:[0,1,1]
	v_mfma_f32_32x32x16_f16 v[16:31], v[156:159], v[136:139], v[16:31]
	v_pk_mul_f16 v148, v54, v36 op_sel:[0,0] op_sel_hi:[0,1]
	v_pk_mul_f16 v149, v54, v37 op_sel:[0,0] op_sel_hi:[0,1]
	v_pk_mul_f16 v150, v54, v38 op_sel:[0,0] op_sel_hi:[0,1]
	v_pk_mul_f16 v151, v54, v39 op_sel:[0,0] op_sel_hi:[0,1]
	v_mfma_f32_32x32x16_f16 v[0:15], v[156:159], v[140:143], v[0:15]
	v_pk_fma_f16 v148, v46, v32, v148 op_sel:[0,0,0] op_sel_hi:[0,1,1] neg_lo:[0,0,1] neg_hi:[0,0,1]
	v_pk_fma_f16 v149, v46, v33, v149 op_sel:[0,0,0] op_sel_hi:[0,1,1] neg_lo:[0,0,1] neg_hi:[0,0,1]
	v_pk_fma_f16 v150, v46, v34, v150 op_sel:[0,0,0] op_sel_hi:[0,1,1] neg_lo:[0,0,1] neg_hi:[0,0,1]
	v_pk_fma_f16 v151, v46, v35, v151 op_sel:[0,0,0] op_sel_hi:[0,1,1] neg_lo:[0,0,1] neg_hi:[0,0,1]
	ds_read_b128 v[96:99], v161 offset:4096
	ds_read_b128 v[100:103], v161 offset:5120
	ds_read_b128 v[104:107], v161 offset:6144
	ds_read_b128 v[108:111], v161 offset:7168
	s_add_u32 s17, s17, 1
	s_cmp_eq_u32 s17, 17
	s_cbranch_scc1 .Lk2_epi

.Lk2_b03:
	s_waitcnt lgkmcnt(4)
	v_mfma_f32_32x32x16_f16 v[16:31], v[144:147], v[80:83], v[16:31]
	s_cmp_le_u32 s22, 16
	s_cselect_b32 s40, s18, 0x18000
	s_add_u32 m0, s40, s35
	v_pk_mul_f16 v152, v54, v32 op_sel:[1,0] op_sel_hi:[1,1]
	v_pk_mul_f16 v153, v54, v33 op_sel:[1,0] op_sel_hi:[1,1]
	v_pk_mul_f16 v154, v54, v34 op_sel:[1,0] op_sel_hi:[1,1]
	v_pk_mul_f16 v155, v54, v35 op_sel:[1,0] op_sel_hi:[1,1]
	v_mfma_f32_32x32x16_f16 v[0:15], v[144:147], v[84:87], v[0:15]
	s_add_u32 s22, s22, 1
	global_load_lds_dwordx4 v168, s[20:21]
	global_load_lds_dwordx4 v168, s[20:21] offset:1024
	v_pk_fma_f16 v152, v46, v36, v152 op_sel:[1,0,0] op_sel_hi:[1,1,1]
	v_pk_fma_f16 v153, v46, v37, v153 op_sel:[1,0,0] op_sel_hi:[1,1,1]
	v_pk_fma_f16 v154, v46, v38, v154 op_sel:[1,0,0] op_sel_hi:[1,1,1]
	v_pk_fma_f16 v155, v46, v39, v155 op_sel:[1,0,0] op_sel_hi:[1,1,1]
	v_mfma_f32_32x32x16_f16 v[16:31], v[148:151], v[88:91], v[16:31]
	s_cmp_le_u32 s22, 16
	s_cselect_b32 s41, 0x4000, 0
	v_pk_mul_f16 v156, v54, v36 op_sel:[1,0] op_sel_hi:[1,1]
	v_pk_mul_f16 v157, v54, v37 op_sel:[1,0] op_sel_hi:[1,1]
	v_pk_mul_f16 v158, v54, v38 op_sel:[1,0] op_sel_hi:[1,1]
	v_pk_mul_f16 v159, v54, v39 op_sel:[1,0] op_sel_hi:[1,1]
	v_mfma_f32_32x32x16_f16 v[0:15], v[148:151], v[92:95], v[0:15]
	s_add_u32 s20, s20, s41
	s_addc_u32 s21, s21, 0
	v_pk_fma_f16 v156, v46, v32, v156 op_sel:[1,0,0] op_sel_hi:[1,1,1] neg_lo:[0,0,1] neg_hi:[0,0,1]
	v_pk_fma_f16 v157, v46, v33, v157 op_sel:[1,0,0] op_sel_hi:[1,1,1] neg_lo:[0,0,1] neg_hi:[0,0,1]
	v_pk_fma_f16 v158, v46, v34, v158 op_sel:[1,0,0] op_sel_hi:[1,1,1] neg_lo:[0,0,1] neg_hi:[0,0,1]
	v_pk_fma_f16 v159, v46, v35, v159 op_sel:[1,0,0] op_sel_hi:[1,1,1] neg_lo:[0,0,1] neg_hi:[0,0,1]
	ds_read_b128 v[112:115], v161 offset:8192
	ds_read_b128 v[116:119], v161 offset:9216
	ds_read_b128 v[120:123], v161 offset:10240
	ds_read_b128 v[124:127], v161 offset:11264
	s_waitcnt lgkmcnt(4)
	v_mfma_f32_32x32x16_f16 v[16:31], v[152:155], v[96:99], v[16:31]
	s_add_u32 s18, s18, 0x4000
	s_cmp_eq_u32 s18, 0x18000
	s_cselect_b32 s18, 0, s18
	v_pk_mul_f16 v144, v55, v32 op_sel:[0,0] op_sel_hi:[0,1]
	v_pk_mul_f16 v145, v55, v33 op_sel:[0,0] op_sel_hi:[0,1]
	v_pk_mul_f16 v146, v55, v34 op_sel:[0,0] op_sel_hi:[0,1]
	v_pk_mul_f16 v147, v55, v35 op_sel:[0,0] op_sel_hi:[0,1]
	v_mfma_f32_32x32x16_f16 v[0:15], v[152:155], v[100:103], v[0:15]
	v_pk_fma_f16 v144, v47, v36, v144 op_sel:[0,0,0] op_sel_hi:[0,1,1]
	v_pk_fma_f16 v145, v47, v37, v145 op_sel:[0,0,0] op_sel_hi:[0,1,1]
	v_pk_fma_f16 v146, v47, v38, v146 op_sel:[0,0,0] op_sel_hi:[0,1,1]
	v_pk_fma_f16 v147, v47, v39, v147 op_sel:[0,0,0] op_sel_hi:[0,1,1]
	v_mfma_f32_32x32x16_f16 v[16:31], v[156:159], v[104:107], v[16:31]
	v_pk_mul_f16 v148, v55, v36 op_sel:[0,0] op_sel_hi:[0,1]
	v_pk_mul_f16 v149, v55, v37 op_sel:[0,0] op_sel_hi:[0,1]
	v_pk_mul_f16 v150, v55, v38 op_sel:[0,0] op_sel_hi:[0,1]
	v_pk_mul_f16 v151, v55, v39 op_sel:[0,0] op_sel_hi:[0,1]
	v_mfma_f32_32x32x16_f16 v[0:15], v[156:159], v[108:111], v[0:15]
	v_pk_fma_f16 v148, v47, v32, v148 op_sel:[0,0,0] op_sel_hi:[0,1,1] neg_lo:[0,0,1] neg_hi:[0,0,1]
	v_pk_fma_f16 v149, v47, v33, v149 op_sel:[0,0,0] op_sel_hi:[0,1,1] neg_lo:[0,0,1] neg_hi:[0,0,1]
	v_pk_fma_f16 v150, v47, v34, v150 op_sel:[0,0,0] op_sel_hi:[0,1,1] neg_lo:[0,0,1] neg_hi:[0,0,1]
	v_pk_fma_f16 v151, v47, v35, v151 op_sel:[0,0,0] op_sel_hi:[0,1,1] neg_lo:[0,0,1] neg_hi:[0,0,1]
	ds_read_b128 v[128:131], v161 offset:12288
	ds_read_b128 v[132:135], v161 offset:13312
	ds_read_b128 v[136:139], v161 offset:14336
	ds_read_b128 v[140:143], v161 offset:15360
	s_add_u32 s19, s19, 0x4000
	s_cmp_eq_u32 s19, 0x18000
	s_cselect_b32 s19, 0, s19
	v_add_u32_e32 v161, s19, v160
	s_waitcnt lgkmcnt(4)
	v_mfma_f32_32x32x16_f16 v[16:31], v[144:147], v[112:115], v[16:31]
	v_pk_mul_f16 v152, v55, v32 op_sel:[1,0] op_sel_hi:[1,1]
	v_pk_mul_f16 v153, v55, v33 op_sel:[1,0] op_sel_hi:[1,1]
	v_pk_mul_f16 v154, v55, v34 op_sel:[1,0] op_sel_hi:[1,1]
	v_pk_mul_f16 v155, v55, v35 op_sel:[1,0] op_sel_hi:[1,1]
	v_mfma_f32_32x32x16_f16 v[0:15], v[144:147], v[116:119], v[0:15]
	v_pk_fma_f16 v152, v47, v36, v152 op_sel:[1,0,0] op_sel_hi:[1,1,1]
	v_pk_fma_f16 v153, v47, v37, v153 op_sel:[1,0,0] op_sel_hi:[1,1,1]
	v_pk_fma_f16 v154, v47, v38, v154 op_sel:[1,0,0] op_sel_hi:[1,1,1]
	v_pk_fma_f16 v155, v47, v39, v155 op_sel:[1,0,0] op_sel_hi:[1,1,1]
	v_mfma_f32_32x32x16_f16 v[16:31], v[148:151], v[120:123], v[16:31]
	v_pk_mul_f16 v156, v55, v36 op_sel:[1,0] op_sel_hi:[1,1]
	v_pk_mul_f16 v157, v55, v37 op_sel:[1,0] op_sel_hi:[1,1]
	v_pk_mul_f16 v158, v55, v38 op_sel:[1,0] op_sel_hi:[1,1]
	v_pk_mul_f16 v159, v55, v39 op_sel:[1,0] op_sel_hi:[1,1]
	v_mfma_f32_32x32x16_f16 v[0:15], v[148:151], v[124:127], v[0:15]
	v_pk_fma_f16 v156, v47, v32, v156 op_sel:[1,0,0] op_sel_hi:[1,1,1] neg_lo:[0,0,1] neg_hi:[0,0,1]
	v_pk_fma_f16 v157, v47, v33, v157 op_sel:[1,0,0] op_sel_hi:[1,1,1] neg_lo:[0,0,1] neg_hi:[0,0,1]
	v_pk_fma_f16 v158, v47, v34, v158 op_sel:[1,0,0] op_sel_hi:[1,1,1] neg_lo:[0,0,1] neg_hi:[0,0,1]
	v_pk_fma_f16 v159, v47, v35, v159 op_sel:[1,0,0] op_sel_hi:[1,1,1] neg_lo:[0,0,1] neg_hi:[0,0,1]
	ds_read_b128 v[80:83], v161
	ds_read_b128 v[84:87], v161 offset:1024
	ds_read_b128 v[88:91], v161 offset:2048
	ds_read_b128 v[92:95], v161 offset:3072
	s_waitcnt lgkmcnt(4)
	v_mfma_f32_32x32x16_f16 v[16:31], v[152:155], v[128:131], v[16:31]
	s_waitcnt vmcnt(6)
	v_pk_mul_f16 v144, v72, v56 op_sel:[0,0] op_sel_hi:[0,1]
	v_pk_mul_f16 v145, v72, v57 op_sel:[0,0] op_sel_hi:[0,1]
	v_pk_mul_f16 v146, v72, v58 op_sel:[0,0] op_sel_hi:[0,1]
	v_pk_mul_f16 v147, v72, v59 op_sel:[0,0] op_sel_hi:[0,1]
	v_mfma_f32_32x32x16_f16 v[0:15], v[152:155], v[132:135], v[0:15]
	v_pk_fma_f16 v144, v64, v60, v144 op_sel:[0,0,0] op_sel_hi:[0,1,1]
	v_pk_fma_f16 v145, v64, v61, v145 op_sel:[0,0,0] op_sel_hi:[0,1,1]
	v_pk_fma_f16 v146, v64, v62, v146 op_sel:[0,0,0] op_sel_hi:[0,1,1]
	v_pk_fma_f16 v147, v64, v63, v147 op_sel:[0,0,0] op_sel_hi:[0,1,1]
	v_mfma_f32_32x32x16_f16 v[16:31], v[156:159], v[136:139], v[16:31]
	v_pk_mul_f16 v148, v72, v60 op_sel:[0,0] op_sel_hi:[0,1]
	v_pk_mul_f16 v149, v72, v61 op_sel:[0,0] op_sel_hi:[0,1]
	v_pk_mul_f16 v150, v72, v62 op_sel:[0,0] op_sel_hi:[0,1]
	v_pk_mul_f16 v151, v72, v63 op_sel:[0,0] op_sel_hi:[0,1]
	v_mfma_f32_32x32x16_f16 v[0:15], v[156:159], v[140:143], v[0:15]
	v_pk_fma_f16 v148, v64, v56, v148 op_sel:[0,0,0] op_sel_hi:[0,1,1] neg_lo:[0,0,1] neg_hi:[0,0,1]
	v_pk_fma_f16 v149, v64, v57, v149 op_sel:[0,0,0] op_sel_hi:[0,1,1] neg_lo:[0,0,1] neg_hi:[0,0,1]
	v_pk_fma_f16 v150, v64, v58, v150 op_sel:[0,0,0] op_sel_hi:[0,1,1] neg_lo:[0,0,1] neg_hi:[0,0,1]
	v_pk_fma_f16 v151, v64, v59, v151 op_sel:[0,0,0] op_sel_hi:[0,1,1] neg_lo:[0,0,1] neg_hi:[0,0,1]
	ds_read_b128 v[96:99], v161 offset:4096
	ds_read_b128 v[100:103], v161 offset:5120
	ds_read_b128 v[104:107], v161 offset:6144
	ds_read_b128 v[108:111], v161 offset:7168
	s_add_u32 s17, s17, 1
	s_cmp_eq_u32 s17, 17
	s_cbranch_scc1 .Lk2_epi

.Lk2_b10:
	s_waitcnt lgkmcnt(4)
	v_mfma_f32_32x32x16_f16 v[16:31], v[144:147], v[80:83], v[16:31]
	s_cmp_le_u32 s22, 16
	s_cselect_b32 s40, s18, 0x18000
	s_add_u32 m0, s40, s35
	s_add_u32 s22, s22, 1
	global_load_lds_dwordx4 v168, s[20:21]
	global_load_lds_dwordx4 v168, s[20:21] offset:1024
	v_pk_mul_f16 v152, v72, v56 op_sel:[1,0] op_sel_hi:[1,1]
	v_pk_mul_f16 v153, v72, v57 op_sel:[1,0] op_sel_hi:[1,1]
	v_pk_mul_f16 v154, v72, v58 op_sel:[1,0] op_sel_hi:[1,1]
	v_pk_mul_f16 v155, v72, v59 op_sel:[1,0] op_sel_hi:[1,1]
	v_mfma_f32_32x32x16_f16 v[0:15], v[144:147], v[84:87], v[0:15]
	s_cmp_le_u32 s22, 16
	s_cselect_b32 s41, 0x4000, 0
	v_pk_fma_f16 v152, v64, v60, v152 op_sel:[1,0,0] op_sel_hi:[1,1,1]
	v_pk_fma_f16 v153, v64, v61, v153 op_sel:[1,0,0] op_sel_hi:[1,1,1]
	v_pk_fma_f16 v154, v64, v62, v154 op_sel:[1,0,0] op_sel_hi:[1,1,1]
	v_pk_fma_f16 v155, v64, v63, v155 op_sel:[1,0,0] op_sel_hi:[1,1,1]
	v_mfma_f32_32x32x16_f16 v[16:31], v[148:151], v[88:91], v[16:31]
	s_add_u32 s20, s20, s41
	s_addc_u32 s21, s21, 0
	v_pk_mul_f16 v156, v72, v60 op_sel:[1,0] op_sel_hi:[1,1]
	v_pk_mul_f16 v157, v72, v61 op_sel:[1,0] op_sel_hi:[1,1]
	v_pk_mul_f16 v158, v72, v62 op_sel:[1,0] op_sel_hi:[1,1]
	v_pk_mul_f16 v159, v72, v63 op_sel:[1,0] op_sel_hi:[1,1]
	v_mfma_f32_32x32x16_f16 v[0:15], v[148:151], v[92:95], v[0:15]
	s_add_u32 s18, s18, 0x4000
	s_cmp_eq_u32 s18, 0x18000
	s_cselect_b32 s18, 0, s18
	v_pk_fma_f16 v156, v64, v56, v156 op_sel:[1,0,0] op_sel_hi:[1,1,1] neg_lo:[0,0,1] neg_hi:[0,0,1]
	v_pk_fma_f16 v157, v64, v57, v157 op_sel:[1,0,0] op_sel_hi:[1,1,1] neg_lo:[0,0,1] neg_hi:[0,0,1]
	v_pk_fma_f16 v158, v64, v58, v158 op_sel:[1,0,0] op_sel_hi:[1,1,1] neg_lo:[0,0,1] neg_hi:[0,0,1]
	v_pk_fma_f16 v159, v64, v59, v159 op_sel:[1,0,0] op_sel_hi:[1,1,1] neg_lo:[0,0,1] neg_hi:[0,0,1]
	ds_read_b128 v[112:115], v161 offset:8192
	ds_read_b128 v[116:119], v161 offset:9216
	ds_read_b128 v[120:123], v161 offset:10240
	ds_read_b128 v[124:127], v161 offset:11264
	s_waitcnt lgkmcnt(4)
	v_mfma_f32_32x32x16_f16 v[16:31], v[152:155], v[96:99], v[16:31]
	s_add_u32 s14, s14, 1
	s_cmp_eq_u32 s14, 16
	s_cselect_b32 s42, 1, 0
	v_pk_mul_f16 v144, v73, v56 op_sel:[0,0] op_sel_hi:[0,1]
	v_pk_mul_f16 v145, v73, v57 op_sel:[0,0] op_sel_hi:[0,1]
	v_pk_mul_f16 v146, v73, v58 op_sel:[0,0] op_sel_hi:[0,1]
	v_pk_mul_f16 v147, v73, v59 op_sel:[0,0] op_sel_hi:[0,1]
	v_mfma_f32_32x32x16_f16 v[0:15], v[152:155], v[100:103], v[0:15]
	s_add_u32 s13, s13, s42
	s_cmp_eq_u32 s42, 1
	s_cselect_b32 s14, s13, s14
	v_pk_fma_f16 v144, v65, v60, v144 op_sel:[0,0,0] op_sel_hi:[0,1,1]
	v_pk_fma_f16 v145, v65, v61, v145 op_sel:[0,0,0] op_sel_hi:[0,1,1]
	v_pk_fma_f16 v146, v65, v62, v146 op_sel:[0,0,0] op_sel_hi:[0,1,1]
	v_pk_fma_f16 v147, v65, v63, v147 op_sel:[0,0,0] op_sel_hi:[0,1,1]
	v_mfma_f32_32x32x16_f16 v[16:31], v[156:159], v[104:107], v[16:31]
	s_min_u32 s43, s13, 15
	s_min_u32 s44, s14, 15
	s_lshl_b32 s45, s44, 16
	v_pk_mul_f16 v148, v73, v60 op_sel:[0,0] op_sel_hi:[0,1]
	v_pk_mul_f16 v149, v73, v61 op_sel:[0,0] op_sel_hi:[0,1]
	v_pk_mul_f16 v150, v73, v62 op_sel:[0,0] op_sel_hi:[0,1]
	v_pk_mul_f16 v151, v73, v63 op_sel:[0,0] op_sel_hi:[0,1]
	v_mfma_f32_32x32x16_f16 v[0:15], v[156:159], v[108:111], v[0:15]
	s_add_u32 s24, s8, s45
	s_addc_u32 s25, s9, 0
	v_pk_fma_f16 v148, v65, v56, v148 op_sel:[0,0,0] op_sel_hi:[0,1,1] neg_lo:[0,0,1] neg_hi:[0,0,1]
	v_pk_fma_f16 v149, v65, v57, v149 op_sel:[0,0,0] op_sel_hi:[0,1,1] neg_lo:[0,0,1] neg_hi:[0,0,1]
	v_pk_fma_f16 v150, v65, v58, v150 op_sel:[0,0,0] op_sel_hi:[0,1,1] neg_lo:[0,0,1] neg_hi:[0,0,1]
	v_pk_fma_f16 v151, v65, v59, v151 op_sel:[0,0,0] op_sel_hi:[0,1,1] neg_lo:[0,0,1] neg_hi:[0,0,1]
	ds_read_b128 v[128:131], v161 offset:12288
	ds_read_b128 v[132:135], v161 offset:13312
	ds_read_b128 v[136:139], v161 offset:14336
	ds_read_b128 v[140:143], v161 offset:15360
	s_add_u32 s19, s19, 0x4000
	s_cmp_eq_u32 s19, 0x18000
	s_cselect_b32 s19, 0, s19
	v_add_u32_e32 v161, s19, v160
	s_waitcnt lgkmcnt(4)
	v_mfma_f32_32x32x16_f16 v[16:31], v[144:147], v[112:115], v[16:31]
	s_add_u32 s26, s24, 0x100000
	s_addc_u32 s27, s25, 0
	s_lshl_b32 s45, s43, 16
	s_add_u32 s28, s8, s45
	s_addc_u32 s29, s9, 0
	v_pk_mul_f16 v152, v73, v56 op_sel:[1,0] op_sel_hi:[1,1]
	v_pk_mul_f16 v153, v73, v57 op_sel:[1,0] op_sel_hi:[1,1]
	v_pk_mul_f16 v154, v73, v58 op_sel:[1,0] op_sel_hi:[1,1]
	v_pk_mul_f16 v155, v73, v59 op_sel:[1,0] op_sel_hi:[1,1]
	v_mfma_f32_32x32x16_f16 v[0:15], v[144:147], v[116:119], v[0:15]
	s_add_u32 s30, s28, 0x100000
	s_addc_u32 s31, s29, 0
	v_pk_fma_f16 v152, v65, v60, v152 op_sel:[1,0,0] op_sel_hi:[1,1,1]
	v_pk_fma_f16 v153, v65, v61, v153 op_sel:[1,0,0] op_sel_hi:[1,1,1]
	v_pk_fma_f16 v154, v65, v62, v154 op_sel:[1,0,0] op_sel_hi:[1,1,1]
	v_pk_fma_f16 v155, v65, v63, v155 op_sel:[1,0,0] op_sel_hi:[1,1,1]
	v_mfma_f32_32x32x16_f16 v[16:31], v[148:151], v[120:123], v[16:31]
	global_load_dwordx4 v[36:39], v164, s[24:25]
	v_pk_mul_f16 v156, v73, v60 op_sel:[1,0] op_sel_hi:[1,1]
	v_pk_mul_f16 v157, v73, v61 op_sel:[1,0] op_sel_hi:[1,1]
	v_pk_mul_f16 v158, v73, v62 op_sel:[1,0] op_sel_hi:[1,1]
	v_pk_mul_f16 v159, v73, v63 op_sel:[1,0] op_sel_hi:[1,1]
	v_mfma_f32_32x32x16_f16 v[0:15], v[148:151], v[124:127], v[0:15]
	global_load_dwordx4 v[32:35], v164, s[26:27]
	v_pk_fma_f16 v156, v65, v56, v156 op_sel:[1,0,0] op_sel_hi:[1,1,1] neg_lo:[0,0,1] neg_hi:[0,0,1]
	v_pk_fma_f16 v157, v65, v57, v157 op_sel:[1,0,0] op_sel_hi:[1,1,1] neg_lo:[0,0,1] neg_hi:[0,0,1]
	v_pk_fma_f16 v158, v65, v58, v158 op_sel:[1,0,0] op_sel_hi:[1,1,1] neg_lo:[0,0,1] neg_hi:[0,0,1]
	v_pk_fma_f16 v159, v65, v59, v159 op_sel:[1,0,0] op_sel_hi:[1,1,1] neg_lo:[0,0,1] neg_hi:[0,0,1]
	ds_read_b128 v[80:83], v161
	ds_read_b128 v[84:87], v161 offset:1024
	ds_read_b128 v[88:91], v161 offset:2048
	ds_read_b128 v[92:95], v161 offset:3072
	s_waitcnt lgkmcnt(4)
	v_mfma_f32_32x32x16_f16 v[16:31], v[152:155], v[128:131], v[16:31]
	global_load_dwordx4 v[40:43], v165, s[28:29]
	v_pk_mul_f16 v144, v74, v56 op_sel:[0,0] op_sel_hi:[0,1]
	v_pk_mul_f16 v145, v74, v57 op_sel:[0,0] op_sel_hi:[0,1]
	v_pk_mul_f16 v146, v74, v58 op_sel:[0,0] op_sel_hi:[0,1]
	v_pk_mul_f16 v147, v74, v59 op_sel:[0,0] op_sel_hi:[0,1]
	v_mfma_f32_32x32x16_f16 v[0:15], v[152:155], v[132:135], v[0:15]
	global_load_dwordx4 v[44:47], v166, s[28:29]
	v_pk_fma_f16 v144, v66, v60, v144 op_sel:[0,0,0] op_sel_hi:[0,1,1]
	v_pk_fma_f16 v145, v66, v61, v145 op_sel:[0,0,0] op_sel_hi:[0,1,1]
	v_pk_fma_f16 v146, v66, v62, v146 op_sel:[0,0,0] op_sel_hi:[0,1,1]
	v_pk_fma_f16 v147, v66, v63, v147 op_sel:[0,0,0] op_sel_hi:[0,1,1]
	v_mfma_f32_32x32x16_f16 v[16:31], v[156:159], v[136:139], v[16:31]
	global_load_dwordx4 v[48:51], v165, s[30:31]
	v_pk_mul_f16 v148, v74, v60 op_sel:[0,0] op_sel_hi:[0,1]
	v_pk_mul_f16 v149, v74, v61 op_sel:[0,0] op_sel_hi:[0,1]
	v_pk_mul_f16 v150, v74, v62 op_sel:[0,0] op_sel_hi:[0,1]
	v_pk_mul_f16 v151, v74, v63 op_sel:[0,0] op_sel_hi:[0,1]
	v_mfma_f32_32x32x16_f16 v[0:15], v[156:159], v[140:143], v[0:15]
	global_load_dwordx4 v[52:55], v166, s[30:31]
	v_pk_fma_f16 v148, v66, v56, v148 op_sel:[0,0,0] op_sel_hi:[0,1,1] neg_lo:[0,0,1] neg_hi:[0,0,1]
	v_pk_fma_f16 v149, v66, v57, v149 op_sel:[0,0,0] op_sel_hi:[0,1,1] neg_lo:[0,0,1] neg_hi:[0,0,1]
	v_pk_fma_f16 v150, v66, v58, v150 op_sel:[0,0,0] op_sel_hi:[0,1,1] neg_lo:[0,0,1] neg_hi:[0,0,1]
	v_pk_fma_f16 v151, v66, v59, v151 op_sel:[0,0,0] op_sel_hi:[0,1,1] neg_lo:[0,0,1] neg_hi:[0,0,1]
	ds_read_b128 v[96:99], v161 offset:4096
	ds_read_b128 v[100:103], v161 offset:5120
	ds_read_b128 v[104:107], v161 offset:6144
	ds_read_b128 v[108:111], v161 offset:7168
	s_add_u32 s17, s17, 1
	s_cmp_eq_u32 s17, 17
	s_cbranch_scc1 .Lk2_epi

.Lk2_b11:
	s_waitcnt lgkmcnt(4)
	v_mfma_f32_32x32x16_f16 v[16:31], v[144:147], v[80:83], v[16:31]
	s_cmp_le_u32 s22, 16
	s_cselect_b32 s40, s18, 0x18000
	s_add_u32 m0, s40, s35
	v_pk_mul_f16 v152, v74, v56 op_sel:[1,0] op_sel_hi:[1,1]
	v_pk_mul_f16 v153, v74, v57 op_sel:[1,0] op_sel_hi:[1,1]
	v_pk_mul_f16 v154, v74, v58 op_sel:[1,0] op_sel_hi:[1,1]
	v_pk_mul_f16 v155, v74, v59 op_sel:[1,0] op_sel_hi:[1,1]
	v_mfma_f32_32x32x16_f16 v[0:15], v[144:147], v[84:87], v[0:15]
	s_add_u32 s22, s22, 1
	global_load_lds_dwordx4 v168, s[20:21]
	global_load_lds_dwordx4 v168, s[20:21] offset:1024
	v_pk_fma_f16 v152, v66, v60, v152 op_sel:[1,0,0] op_sel_hi:[1,1,1]
	v_pk_fma_f16 v153, v66, v61, v153 op_sel:[1,0,0] op_sel_hi:[1,1,1]
	v_pk_fma_f16 v154, v66, v62, v154 op_sel:[1,0,0] op_sel_hi:[1,1,1]
	v_pk_fma_f16 v155, v66, v63, v155 op_sel:[1,0,0] op_sel_hi:[1,1,1]
	v_mfma_f32_32x32x16_f16 v[16:31], v[148:151], v[88:91], v[16:31]
	s_cmp_le_u32 s22, 16
	s_cselect_b32 s41, 0x4000, 0
	v_pk_mul_f16 v156, v74, v60 op_sel:[1,0] op_sel_hi:[1,1]
	v_pk_mul_f16 v157, v74, v61 op_sel:[1,0] op_sel_hi:[1,1]
	v_pk_mul_f16 v158, v74, v62 op_sel:[1,0] op_sel_hi:[1,1]
	v_pk_mul_f16 v159, v74, v63 op_sel:[1,0] op_sel_hi:[1,1]
	v_mfma_f32_32x32x16_f16 v[0:15], v[148:151], v[92:95], v[0:15]
	s_add_u32 s20, s20, s41
	s_addc_u32 s21, s21, 0
	v_pk_fma_f16 v156, v66, v56, v156 op_sel:[1,0,0] op_sel_hi:[1,1,1] neg_lo:[0,0,1] neg_hi:[0,0,1]
	v_pk_fma_f16 v157, v66, v57, v157 op_sel:[1,0,0] op_sel_hi:[1,1,1] neg_lo:[0,0,1] neg_hi:[0,0,1]
	v_pk_fma_f16 v158, v66, v58, v158 op_sel:[1,0,0] op_sel_hi:[1,1,1] neg_lo:[0,0,1] neg_hi:[0,0,1]
	v_pk_fma_f16 v159, v66, v59, v159 op_sel:[1,0,0] op_sel_hi:[1,1,1] neg_lo:[0,0,1] neg_hi:[0,0,1]
	ds_read_b128 v[112:115], v161 offset:8192
	ds_read_b128 v[116:119], v161 offset:9216
	ds_read_b128 v[120:123], v161 offset:10240
	ds_read_b128 v[124:127], v161 offset:11264
	s_waitcnt lgkmcnt(4)
	v_mfma_f32_32x32x16_f16 v[16:31], v[152:155], v[96:99], v[16:31]
	s_add_u32 s18, s18, 0x4000
	s_cmp_eq_u32 s18, 0x18000
	s_cselect_b32 s18, 0, s18
	v_pk_mul_f16 v144, v75, v56 op_sel:[0,0] op_sel_hi:[0,1]
	v_pk_mul_f16 v145, v75, v57 op_sel:[0,0] op_sel_hi:[0,1]
	v_pk_mul_f16 v146, v75, v58 op_sel:[0,0] op_sel_hi:[0,1]
	v_pk_mul_f16 v147, v75, v59 op_sel:[0,0] op_sel_hi:[0,1]
	v_mfma_f32_32x32x16_f16 v[0:15], v[152:155], v[100:103], v[0:15]
	v_pk_fma_f16 v144, v67, v60, v144 op_sel:[0,0,0] op_sel_hi:[0,1,1]
	v_pk_fma_f16 v145, v67, v61, v145 op_sel:[0,0,0] op_sel_hi:[0,1,1]
	v_pk_fma_f16 v146, v67, v62, v146 op_sel:[0,0,0] op_sel_hi:[0,1,1]
	v_pk_fma_f16 v147, v67, v63, v147 op_sel:[0,0,0] op_sel_hi:[0,1,1]
	v_mfma_f32_32x32x16_f16 v[16:31], v[156:159], v[104:107], v[16:31]
	v_pk_mul_f16 v148, v75, v60 op_sel:[0,0] op_sel_hi:[0,1]
	v_pk_mul_f16 v149, v75, v61 op_sel:[0,0] op_sel_hi:[0,1]
	v_pk_mul_f16 v150, v75, v62 op_sel:[0,0] op_sel_hi:[0,1]
	v_pk_mul_f16 v151, v75, v63 op_sel:[0,0] op_sel_hi:[0,1]
	v_mfma_f32_32x32x16_f16 v[0:15], v[156:159], v[108:111], v[0:15]
	v_pk_fma_f16 v148, v67, v56, v148 op_sel:[0,0,0] op_sel_hi:[0,1,1] neg_lo:[0,0,1] neg_hi:[0,0,1]
	v_pk_fma_f16 v149, v67, v57, v149 op_sel:[0,0,0] op_sel_hi:[0,1,1] neg_lo:[0,0,1] neg_hi:[0,0,1]
	v_pk_fma_f16 v150, v67, v58, v150 op_sel:[0,0,0] op_sel_hi:[0,1,1] neg_lo:[0,0,1] neg_hi:[0,0,1]
	v_pk_fma_f16 v151, v67, v59, v151 op_sel:[0,0,0] op_sel_hi:[0,1,1] neg_lo:[0,0,1] neg_hi:[0,0,1]
	ds_read_b128 v[128:131], v161 offset:12288
	ds_read_b128 v[132:135], v161 offset:13312
	ds_read_b128 v[136:139], v161 offset:14336
	ds_read_b128 v[140:143], v161 offset:15360
	s_add_u32 s19, s19, 0x4000
	s_cmp_eq_u32 s19, 0x18000
	s_cselect_b32 s19, 0, s19
	v_add_u32_e32 v161, s19, v160
	s_waitcnt lgkmcnt(4)
	v_mfma_f32_32x32x16_f16 v[16:31], v[144:147], v[112:115], v[16:31]
	v_pk_mul_f16 v152, v75, v56 op_sel:[1,0] op_sel_hi:[1,1]
	v_pk_mul_f16 v153, v75, v57 op_sel:[1,0] op_sel_hi:[1,1]
	v_pk_mul_f16 v154, v75, v58 op_sel:[1,0] op_sel_hi:[1,1]
	v_pk_mul_f16 v155, v75, v59 op_sel:[1,0] op_sel_hi:[1,1]
	v_mfma_f32_32x32x16_f16 v[0:15], v[144:147], v[116:119], v[0:15]
	v_pk_fma_f16 v152, v67, v60, v152 op_sel:[1,0,0] op_sel_hi:[1,1,1]
	v_pk_fma_f16 v153, v67, v61, v153 op_sel:[1,0,0] op_sel_hi:[1,1,1]
	v_pk_fma_f16 v154, v67, v62, v154 op_sel:[1,0,0] op_sel_hi:[1,1,1]
	v_pk_fma_f16 v155, v67, v63, v155 op_sel:[1,0,0] op_sel_hi:[1,1,1]
	v_mfma_f32_32x32x16_f16 v[16:31], v[148:151], v[120:123], v[16:31]
	v_pk_mul_f16 v156, v75, v60 op_sel:[1,0] op_sel_hi:[1,1]
	v_pk_mul_f16 v157, v75, v61 op_sel:[1,0] op_sel_hi:[1,1]
	v_pk_mul_f16 v158, v75, v62 op_sel:[1,0] op_sel_hi:[1,1]
	v_pk_mul_f16 v159, v75, v63 op_sel:[1,0] op_sel_hi:[1,1]
	v_mfma_f32_32x32x16_f16 v[0:15], v[148:151], v[124:127], v[0:15]
	v_pk_fma_f16 v156, v67, v56, v156 op_sel:[1,0,0] op_sel_hi:[1,1,1] neg_lo:[0,0,1] neg_hi:[0,0,1]
	v_pk_fma_f16 v157, v67, v57, v157 op_sel:[1,0,0] op_sel_hi:[1,1,1] neg_lo:[0,0,1] neg_hi:[0,0,1]
	v_pk_fma_f16 v158, v67, v58, v158 op_sel:[1,0,0] op_sel_hi:[1,1,1] neg_lo:[0,0,1] neg_hi:[0,0,1]
	v_pk_fma_f16 v159, v67, v59, v159 op_sel:[1,0,0] op_sel_hi:[1,1,1] neg_lo:[0,0,1] neg_hi:[0,0,1]
	ds_read_b128 v[80:83], v161
	ds_read_b128 v[84:87], v161 offset:1024
	ds_read_b128 v[88:91], v161 offset:2048
	ds_read_b128 v[92:95], v161 offset:3072
	s_waitcnt lgkmcnt(4)
	v_mfma_f32_32x32x16_f16 v[16:31], v[152:155], v[128:131], v[16:31]
	v_pk_mul_f16 v144, v76, v56 op_sel:[0,0] op_sel_hi:[0,1]
	v_pk_mul_f16 v145, v76, v57 op_sel:[0,0] op_sel_hi:[0,1]
	v_pk_mul_f16 v146, v76, v58 op_sel:[0,0] op_sel_hi:[0,1]
	v_pk_mul_f16 v147, v76, v59 op_sel:[0,0] op_sel_hi:[0,1]
	v_mfma_f32_32x32x16_f16 v[0:15], v[152:155], v[132:135], v[0:15]
	v_pk_fma_f16 v144, v68, v60, v144 op_sel:[0,0,0] op_sel_hi:[0,1,1]
	v_pk_fma_f16 v145, v68, v61, v145 op_sel:[0,0,0] op_sel_hi:[0,1,1]
	v_pk_fma_f16 v146, v68, v62, v146 op_sel:[0,0,0] op_sel_hi:[0,1,1]
	v_pk_fma_f16 v147, v68, v63, v147 op_sel:[0,0,0] op_sel_hi:[0,1,1]
	v_mfma_f32_32x32x16_f16 v[16:31], v[156:159], v[136:139], v[16:31]
	v_pk_mul_f16 v148, v76, v60 op_sel:[0,0] op_sel_hi:[0,1]
	v_pk_mul_f16 v149, v76, v61 op_sel:[0,0] op_sel_hi:[0,1]
	v_pk_mul_f16 v150, v76, v62 op_sel:[0,0] op_sel_hi:[0,1]
	v_pk_mul_f16 v151, v76, v63 op_sel:[0,0] op_sel_hi:[0,1]
	v_mfma_f32_32x32x16_f16 v[0:15], v[156:159], v[140:143], v[0:15]
	v_pk_fma_f16 v148, v68, v56, v148 op_sel:[0,0,0] op_sel_hi:[0,1,1] neg_lo:[0,0,1] neg_hi:[0,0,1]
	v_pk_fma_f16 v149, v68, v57, v149 op_sel:[0,0,0] op_sel_hi:[0,1,1] neg_lo:[0,0,1] neg_hi:[0,0,1]
	v_pk_fma_f16 v150, v68, v58, v150 op_sel:[0,0,0] op_sel_hi:[0,1,1] neg_lo:[0,0,1] neg_hi:[0,0,1]
	v_pk_fma_f16 v151, v68, v59, v151 op_sel:[0,0,0] op_sel_hi:[0,1,1] neg_lo:[0,0,1] neg_hi:[0,0,1]
	ds_read_b128 v[96:99], v161 offset:4096
	ds_read_b128 v[100:103], v161 offset:5120
	ds_read_b128 v[104:107], v161 offset:6144
	ds_read_b128 v[108:111], v161 offset:7168
	s_add_u32 s17, s17, 1
	s_cmp_eq_u32 s17, 17
	s_cbranch_scc1 .Lk2_epi

.Lk2_b12:
	s_waitcnt lgkmcnt(4)
	v_mfma_f32_32x32x16_f16 v[16:31], v[144:147], v[80:83], v[16:31]
	s_cmp_le_u32 s22, 16
	s_cselect_b32 s40, s18, 0x18000
	s_add_u32 m0, s40, s35
	v_pk_mul_f16 v152, v76, v56 op_sel:[1,0] op_sel_hi:[1,1]
	v_pk_mul_f16 v153, v76, v57 op_sel:[1,0] op_sel_hi:[1,1]
	v_pk_mul_f16 v154, v76, v58 op_sel:[1,0] op_sel_hi:[1,1]
	v_pk_mul_f16 v155, v76, v59 op_sel:[1,0] op_sel_hi:[1,1]
	v_mfma_f32_32x32x16_f16 v[0:15], v[144:147], v[84:87], v[0:15]
	s_add_u32 s22, s22, 1
	global_load_lds_dwordx4 v168, s[20:21]
	global_load_lds_dwordx4 v168, s[20:21] offset:1024
	v_pk_fma_f16 v152, v68, v60, v152 op_sel:[1,0,0] op_sel_hi:[1,1,1]
	v_pk_fma_f16 v153, v68, v61, v153 op_sel:[1,0,0] op_sel_hi:[1,1,1]
	v_pk_fma_f16 v154, v68, v62, v154 op_sel:[1,0,0] op_sel_hi:[1,1,1]
	v_pk_fma_f16 v155, v68, v63, v155 op_sel:[1,0,0] op_sel_hi:[1,1,1]
	v_mfma_f32_32x32x16_f16 v[16:31], v[148:151], v[88:91], v[16:31]
	s_cmp_le_u32 s22, 16
	s_cselect_b32 s41, 0x4000, 0
	v_pk_mul_f16 v156, v76, v60 op_sel:[1,0] op_sel_hi:[1,1]
	v_pk_mul_f16 v157, v76, v61 op_sel:[1,0] op_sel_hi:[1,1]
	v_pk_mul_f16 v158, v76, v62 op_sel:[1,0] op_sel_hi:[1,1]
	v_pk_mul_f16 v159, v76, v63 op_sel:[1,0] op_sel_hi:[1,1]
	v_mfma_f32_32x32x16_f16 v[0:15], v[148:151], v[92:95], v[0:15]
	s_add_u32 s20, s20, s41
	s_addc_u32 s21, s21, 0
	v_pk_fma_f16 v156, v68, v56, v156 op_sel:[1,0,0] op_sel_hi:[1,1,1] neg_lo:[0,0,1] neg_hi:[0,0,1]
	v_pk_fma_f16 v157, v68, v57, v157 op_sel:[1,0,0] op_sel_hi:[1,1,1] neg_lo:[0,0,1] neg_hi:[0,0,1]
	v_pk_fma_f16 v158, v68, v58, v158 op_sel:[1,0,0] op_sel_hi:[1,1,1] neg_lo:[0,0,1] neg_hi:[0,0,1]
	v_pk_fma_f16 v159, v68, v59, v159 op_sel:[1,0,0] op_sel_hi:[1,1,1] neg_lo:[0,0,1] neg_hi:[0,0,1]
	ds_read_b128 v[112:115], v161 offset:8192
	ds_read_b128 v[116:119], v161 offset:9216
	ds_read_b128 v[120:123], v161 offset:10240
	ds_read_b128 v[124:127], v161 offset:11264
	s_waitcnt lgkmcnt(4)
	v_mfma_f32_32x32x16_f16 v[16:31], v[152:155], v[96:99], v[16:31]
	s_add_u32 s18, s18, 0x4000
	s_cmp_eq_u32 s18, 0x18000
	s_cselect_b32 s18, 0, s18
	v_pk_mul_f16 v144, v77, v56 op_sel:[0,0] op_sel_hi:[0,1]
	v_pk_mul_f16 v145, v77, v57 op_sel:[0,0] op_sel_hi:[0,1]
	v_pk_mul_f16 v146, v77, v58 op_sel:[0,0] op_sel_hi:[0,1]
	v_pk_mul_f16 v147, v77, v59 op_sel:[0,0] op_sel_hi:[0,1]
	v_mfma_f32_32x32x16_f16 v[0:15], v[152:155], v[100:103], v[0:15]
	v_pk_fma_f16 v144, v69, v60, v144 op_sel:[0,0,0] op_sel_hi:[0,1,1]
	v_pk_fma_f16 v145, v69, v61, v145 op_sel:[0,0,0] op_sel_hi:[0,1,1]
	v_pk_fma_f16 v146, v69, v62, v146 op_sel:[0,0,0] op_sel_hi:[0,1,1]
	v_pk_fma_f16 v147, v69, v63, v147 op_sel:[0,0,0] op_sel_hi:[0,1,1]
	v_mfma_f32_32x32x16_f16 v[16:31], v[156:159], v[104:107], v[16:31]
	v_pk_mul_f16 v148, v77, v60 op_sel:[0,0] op_sel_hi:[0,1]
	v_pk_mul_f16 v149, v77, v61 op_sel:[0,0] op_sel_hi:[0,1]
	v_pk_mul_f16 v150, v77, v62 op_sel:[0,0] op_sel_hi:[0,1]
	v_pk_mul_f16 v151, v77, v63 op_sel:[0,0] op_sel_hi:[0,1]
	v_mfma_f32_32x32x16_f16 v[0:15], v[156:159], v[108:111], v[0:15]
	v_pk_fma_f16 v148, v69, v56, v148 op_sel:[0,0,0] op_sel_hi:[0,1,1] neg_lo:[0,0,1] neg_hi:[0,0,1]
	v_pk_fma_f16 v149, v69, v57, v149 op_sel:[0,0,0] op_sel_hi:[0,1,1] neg_lo:[0,0,1] neg_hi:[0,0,1]
	v_pk_fma_f16 v150, v69, v58, v150 op_sel:[0,0,0] op_sel_hi:[0,1,1] neg_lo:[0,0,1] neg_hi:[0,0,1]
	v_pk_fma_f16 v151, v69, v59, v151 op_sel:[0,0,0] op_sel_hi:[0,1,1] neg_lo:[0,0,1] neg_hi:[0,0,1]
	ds_read_b128 v[128:131], v161 offset:12288
	ds_read_b128 v[132:135], v161 offset:13312
	ds_read_b128 v[136:139], v161 offset:14336
	ds_read_b128 v[140:143], v161 offset:15360
	s_add_u32 s19, s19, 0x4000
	s_cmp_eq_u32 s19, 0x18000
	s_cselect_b32 s19, 0, s19
	v_add_u32_e32 v161, s19, v160
	s_waitcnt lgkmcnt(4)
	v_mfma_f32_32x32x16_f16 v[16:31], v[144:147], v[112:115], v[16:31]
	v_pk_mul_f16 v152, v77, v56 op_sel:[1,0] op_sel_hi:[1,1]
	v_pk_mul_f16 v153, v77, v57 op_sel:[1,0] op_sel_hi:[1,1]
	v_pk_mul_f16 v154, v77, v58 op_sel:[1,0] op_sel_hi:[1,1]
	v_pk_mul_f16 v155, v77, v59 op_sel:[1,0] op_sel_hi:[1,1]
	v_mfma_f32_32x32x16_f16 v[0:15], v[144:147], v[116:119], v[0:15]
	v_pk_fma_f16 v152, v69, v60, v152 op_sel:[1,0,0] op_sel_hi:[1,1,1]
	v_pk_fma_f16 v153, v69, v61, v153 op_sel:[1,0,0] op_sel_hi:[1,1,1]
	v_pk_fma_f16 v154, v69, v62, v154 op_sel:[1,0,0] op_sel_hi:[1,1,1]
	v_pk_fma_f16 v155, v69, v63, v155 op_sel:[1,0,0] op_sel_hi:[1,1,1]
	v_mfma_f32_32x32x16_f16 v[16:31], v[148:151], v[120:123], v[16:31]
	v_pk_mul_f16 v156, v77, v60 op_sel:[1,0] op_sel_hi:[1,1]
	v_pk_mul_f16 v157, v77, v61 op_sel:[1,0] op_sel_hi:[1,1]
	v_pk_mul_f16 v158, v77, v62 op_sel:[1,0] op_sel_hi:[1,1]
	v_pk_mul_f16 v159, v77, v63 op_sel:[1,0] op_sel_hi:[1,1]
	v_mfma_f32_32x32x16_f16 v[0:15], v[148:151], v[124:127], v[0:15]
	v_pk_fma_f16 v156, v69, v56, v156 op_sel:[1,0,0] op_sel_hi:[1,1,1] neg_lo:[0,0,1] neg_hi:[0,0,1]
	v_pk_fma_f16 v157, v69, v57, v157 op_sel:[1,0,0] op_sel_hi:[1,1,1] neg_lo:[0,0,1] neg_hi:[0,0,1]
	v_pk_fma_f16 v158, v69, v58, v158 op_sel:[1,0,0] op_sel_hi:[1,1,1] neg_lo:[0,0,1] neg_hi:[0,0,1]
	v_pk_fma_f16 v159, v69, v59, v159 op_sel:[1,0,0] op_sel_hi:[1,1,1] neg_lo:[0,0,1] neg_hi:[0,0,1]
	ds_read_b128 v[80:83], v161
	ds_read_b128 v[84:87], v161 offset:1024
	ds_read_b128 v[88:91], v161 offset:2048
	ds_read_b128 v[92:95], v161 offset:3072
	s_waitcnt lgkmcnt(4)
	v_mfma_f32_32x32x16_f16 v[16:31], v[152:155], v[128:131], v[16:31]
	v_pk_mul_f16 v144, v78, v56 op_sel:[0,0] op_sel_hi:[0,1]
	v_pk_mul_f16 v145, v78, v57 op_sel:[0,0] op_sel_hi:[0,1]
	v_pk_mul_f16 v146, v78, v58 op_sel:[0,0] op_sel_hi:[0,1]
	v_pk_mul_f16 v147, v78, v59 op_sel:[0,0] op_sel_hi:[0,1]
	v_mfma_f32_32x32x16_f16 v[0:15], v[152:155], v[132:135], v[0:15]
	v_pk_fma_f16 v144, v70, v60, v144 op_sel:[0,0,0] op_sel_hi:[0,1,1]
	v_pk_fma_f16 v145, v70, v61, v145 op_sel:[0,0,0] op_sel_hi:[0,1,1]
	v_pk_fma_f16 v146, v70, v62, v146 op_sel:[0,0,0] op_sel_hi:[0,1,1]
	v_pk_fma_f16 v147, v70, v63, v147 op_sel:[0,0,0] op_sel_hi:[0,1,1]
	v_mfma_f32_32x32x16_f16 v[16:31], v[156:159], v[136:139], v[16:31]
	v_pk_mul_f16 v148, v78, v60 op_sel:[0,0] op_sel_hi:[0,1]
	v_pk_mul_f16 v149, v78, v61 op_sel:[0,0] op_sel_hi:[0,1]
	v_pk_mul_f16 v150, v78, v62 op_sel:[0,0] op_sel_hi:[0,1]
	v_pk_mul_f16 v151, v78, v63 op_sel:[0,0] op_sel_hi:[0,1]
	v_mfma_f32_32x32x16_f16 v[0:15], v[156:159], v[140:143], v[0:15]
	v_pk_fma_f16 v148, v70, v56, v148 op_sel:[0,0,0] op_sel_hi:[0,1,1] neg_lo:[0,0,1] neg_hi:[0,0,1]
	v_pk_fma_f16 v149, v70, v57, v149 op_sel:[0,0,0] op_sel_hi:[0,1,1] neg_lo:[0,0,1] neg_hi:[0,0,1]
	v_pk_fma_f16 v150, v70, v58, v150 op_sel:[0,0,0] op_sel_hi:[0,1,1] neg_lo:[0,0,1] neg_hi:[0,0,1]
	v_pk_fma_f16 v151, v70, v59, v151 op_sel:[0,0,0] op_sel_hi:[0,1,1] neg_lo:[0,0,1] neg_hi:[0,0,1]
	ds_read_b128 v[96:99], v161 offset:4096
	ds_read_b128 v[100:103], v161 offset:5120
	ds_read_b128 v[104:107], v161 offset:6144
	ds_read_b128 v[108:111], v161 offset:7168
	s_add_u32 s17, s17, 1
	s_cmp_eq_u32 s17, 17
	s_cbranch_scc1 .Lk2_epi

.Lk2_b13:
	s_waitcnt lgkmcnt(4)
	v_mfma_f32_32x32x16_f16 v[16:31], v[144:147], v[80:83], v[16:31]
	s_cmp_le_u32 s22, 16
	s_cselect_b32 s40, s18, 0x18000
	s_add_u32 m0, s40, s35
	v_pk_mul_f16 v152, v78, v56 op_sel:[1,0] op_sel_hi:[1,1]
	v_pk_mul_f16 v153, v78, v57 op_sel:[1,0] op_sel_hi:[1,1]
	v_pk_mul_f16 v154, v78, v58 op_sel:[1,0] op_sel_hi:[1,1]
	v_pk_mul_f16 v155, v78, v59 op_sel:[1,0] op_sel_hi:[1,1]
	v_mfma_f32_32x32x16_f16 v[0:15], v[144:147], v[84:87], v[0:15]
	s_add_u32 s22, s22, 1
	global_load_lds_dwordx4 v168, s[20:21]
	global_load_lds_dwordx4 v168, s[20:21] offset:1024
	v_pk_fma_f16 v152, v70, v60, v152 op_sel:[1,0,0] op_sel_hi:[1,1,1]
	v_pk_fma_f16 v153, v70, v61, v153 op_sel:[1,0,0] op_sel_hi:[1,1,1]
	v_pk_fma_f16 v154, v70, v62, v154 op_sel:[1,0,0] op_sel_hi:[1,1,1]
	v_pk_fma_f16 v155, v70, v63, v155 op_sel:[1,0,0] op_sel_hi:[1,1,1]
	v_mfma_f32_32x32x16_f16 v[16:31], v[148:151], v[88:91], v[16:31]
	s_cmp_le_u32 s22, 16
	s_cselect_b32 s41, 0x4000, 0
	v_pk_mul_f16 v156, v78, v60 op_sel:[1,0] op_sel_hi:[1,1]
	v_pk_mul_f16 v157, v78, v61 op_sel:[1,0] op_sel_hi:[1,1]
	v_pk_mul_f16 v158, v78, v62 op_sel:[1,0] op_sel_hi:[1,1]
	v_pk_mul_f16 v159, v78, v63 op_sel:[1,0] op_sel_hi:[1,1]
	v_mfma_f32_32x32x16_f16 v[0:15], v[148:151], v[92:95], v[0:15]
	s_add_u32 s20, s20, s41
	s_addc_u32 s21, s21, 0
	v_pk_fma_f16 v156, v70, v56, v156 op_sel:[1,0,0] op_sel_hi:[1,1,1] neg_lo:[0,0,1] neg_hi:[0,0,1]
	v_pk_fma_f16 v157, v70, v57, v157 op_sel:[1,0,0] op_sel_hi:[1,1,1] neg_lo:[0,0,1] neg_hi:[0,0,1]
	v_pk_fma_f16 v158, v70, v58, v158 op_sel:[1,0,0] op_sel_hi:[1,1,1] neg_lo:[0,0,1] neg_hi:[0,0,1]
	v_pk_fma_f16 v159, v70, v59, v159 op_sel:[1,0,0] op_sel_hi:[1,1,1] neg_lo:[0,0,1] neg_hi:[0,0,1]
	ds_read_b128 v[112:115], v161 offset:8192
	ds_read_b128 v[116:119], v161 offset:9216
	ds_read_b128 v[120:123], v161 offset:10240
	ds_read_b128 v[124:127], v161 offset:11264
	s_waitcnt lgkmcnt(4)
	v_mfma_f32_32x32x16_f16 v[16:31], v[152:155], v[96:99], v[16:31]
	s_add_u32 s18, s18, 0x4000
	s_cmp_eq_u32 s18, 0x18000
	s_cselect_b32 s18, 0, s18
	v_pk_mul_f16 v144, v79, v56 op_sel:[0,0] op_sel_hi:[0,1]
	v_pk_mul_f16 v145, v79, v57 op_sel:[0,0] op_sel_hi:[0,1]
	v_pk_mul_f16 v146, v79, v58 op_sel:[0,0] op_sel_hi:[0,1]
	v_pk_mul_f16 v147, v79, v59 op_sel:[0,0] op_sel_hi:[0,1]
	v_mfma_f32_32x32x16_f16 v[0:15], v[152:155], v[100:103], v[0:15]
	v_pk_fma_f16 v144, v71, v60, v144 op_sel:[0,0,0] op_sel_hi:[0,1,1]
	v_pk_fma_f16 v145, v71, v61, v145 op_sel:[0,0,0] op_sel_hi:[0,1,1]
	v_pk_fma_f16 v146, v71, v62, v146 op_sel:[0,0,0] op_sel_hi:[0,1,1]
	v_pk_fma_f16 v147, v71, v63, v147 op_sel:[0,0,0] op_sel_hi:[0,1,1]
	v_mfma_f32_32x32x16_f16 v[16:31], v[156:159], v[104:107], v[16:31]
	v_pk_mul_f16 v148, v79, v60 op_sel:[0,0] op_sel_hi:[0,1]
	v_pk_mul_f16 v149, v79, v61 op_sel:[0,0] op_sel_hi:[0,1]
	v_pk_mul_f16 v150, v79, v62 op_sel:[0,0] op_sel_hi:[0,1]
	v_pk_mul_f16 v151, v79, v63 op_sel:[0,0] op_sel_hi:[0,1]
	v_mfma_f32_32x32x16_f16 v[0:15], v[156:159], v[108:111], v[0:15]
	v_pk_fma_f16 v148, v71, v56, v148 op_sel:[0,0,0] op_sel_hi:[0,1,1] neg_lo:[0,0,1] neg_hi:[0,0,1]
	v_pk_fma_f16 v149, v71, v57, v149 op_sel:[0,0,0] op_sel_hi:[0,1,1] neg_lo:[0,0,1] neg_hi:[0,0,1]
	v_pk_fma_f16 v150, v71, v58, v150 op_sel:[0,0,0] op_sel_hi:[0,1,1] neg_lo:[0,0,1] neg_hi:[0,0,1]
	v_pk_fma_f16 v151, v71, v59, v151 op_sel:[0,0,0] op_sel_hi:[0,1,1] neg_lo:[0,0,1] neg_hi:[0,0,1]
	ds_read_b128 v[128:131], v161 offset:12288
	ds_read_b128 v[132:135], v161 offset:13312
	ds_read_b128 v[136:139], v161 offset:14336
	ds_read_b128 v[140:143], v161 offset:15360
	s_add_u32 s19, s19, 0x4000
	s_cmp_eq_u32 s19, 0x18000
	s_cselect_b32 s19, 0, s19
	v_add_u32_e32 v161, s19, v160
	s_waitcnt lgkmcnt(4)
	v_mfma_f32_32x32x16_f16 v[16:31], v[144:147], v[112:115], v[16:31]
	v_pk_mul_f16 v152, v79, v56 op_sel:[1,0] op_sel_hi:[1,1]
	v_pk_mul_f16 v153, v79, v57 op_sel:[1,0] op_sel_hi:[1,1]
	v_pk_mul_f16 v154, v79, v58 op_sel:[1,0] op_sel_hi:[1,1]
	v_pk_mul_f16 v155, v79, v59 op_sel:[1,0] op_sel_hi:[1,1]
	v_mfma_f32_32x32x16_f16 v[0:15], v[144:147], v[116:119], v[0:15]
	v_pk_fma_f16 v152, v71, v60, v152 op_sel:[1,0,0] op_sel_hi:[1,1,1]
	v_pk_fma_f16 v153, v71, v61, v153 op_sel:[1,0,0] op_sel_hi:[1,1,1]
	v_pk_fma_f16 v154, v71, v62, v154 op_sel:[1,0,0] op_sel_hi:[1,1,1]
	v_pk_fma_f16 v155, v71, v63, v155 op_sel:[1,0,0] op_sel_hi:[1,1,1]
	v_mfma_f32_32x32x16_f16 v[16:31], v[148:151], v[120:123], v[16:31]
	v_pk_mul_f16 v156, v79, v60 op_sel:[1,0] op_sel_hi:[1,1]
	v_pk_mul_f16 v157, v79, v61 op_sel:[1,0] op_sel_hi:[1,1]
	v_pk_mul_f16 v158, v79, v62 op_sel:[1,0] op_sel_hi:[1,1]
	v_pk_mul_f16 v159, v79, v63 op_sel:[1,0] op_sel_hi:[1,1]
	v_mfma_f32_32x32x16_f16 v[0:15], v[148:151], v[124:127], v[0:15]
	v_pk_fma_f16 v156, v71, v56, v156 op_sel:[1,0,0] op_sel_hi:[1,1,1] neg_lo:[0,0,1] neg_hi:[0,0,1]
	v_pk_fma_f16 v157, v71, v57, v157 op_sel:[1,0,0] op_sel_hi:[1,1,1] neg_lo:[0,0,1] neg_hi:[0,0,1]
	v_pk_fma_f16 v158, v71, v58, v158 op_sel:[1,0,0] op_sel_hi:[1,1,1] neg_lo:[0,0,1] neg_hi:[0,0,1]
	v_pk_fma_f16 v159, v71, v59, v159 op_sel:[1,0,0] op_sel_hi:[1,1,1] neg_lo:[0,0,1] neg_hi:[0,0,1]
	ds_read_b128 v[80:83], v161
	ds_read_b128 v[84:87], v161 offset:1024
	ds_read_b128 v[88:91], v161 offset:2048
	ds_read_b128 v[92:95], v161 offset:3072
	s_waitcnt lgkmcnt(4)
	v_mfma_f32_32x32x16_f16 v[16:31], v[152:155], v[128:131], v[16:31]
	s_waitcnt vmcnt(6)
	v_pk_mul_f16 v144, v48, v32 op_sel:[0,0] op_sel_hi:[0,1]
	v_pk_mul_f16 v145, v48, v33 op_sel:[0,0] op_sel_hi:[0,1]
	v_pk_mul_f16 v146, v48, v34 op_sel:[0,0] op_sel_hi:[0,1]
	v_pk_mul_f16 v147, v48, v35 op_sel:[0,0] op_sel_hi:[0,1]
	v_mfma_f32_32x32x16_f16 v[0:15], v[152:155], v[132:135], v[0:15]
	v_pk_fma_f16 v144, v40, v36, v144 op_sel:[0,0,0] op_sel_hi:[0,1,1]
	v_pk_fma_f16 v145, v40, v37, v145 op_sel:[0,0,0] op_sel_hi:[0,1,1]
	v_pk_fma_f16 v146, v40, v38, v146 op_sel:[0,0,0] op_sel_hi:[0,1,1]
	v_pk_fma_f16 v147, v40, v39, v147 op_sel:[0,0,0] op_sel_hi:[0,1,1]
	v_mfma_f32_32x32x16_f16 v[16:31], v[156:159], v[136:139], v[16:31]
	v_pk_mul_f16 v148, v48, v36 op_sel:[0,0] op_sel_hi:[0,1]
	v_pk_mul_f16 v149, v48, v37 op_sel:[0,0] op_sel_hi:[0,1]
	v_pk_mul_f16 v150, v48, v38 op_sel:[0,0] op_sel_hi:[0,1]
	v_pk_mul_f16 v151, v48, v39 op_sel:[0,0] op_sel_hi:[0,1]
	v_mfma_f32_32x32x16_f16 v[0:15], v[156:159], v[140:143], v[0:15]
	v_pk_fma_f16 v148, v40, v32, v148 op_sel:[0,0,0] op_sel_hi:[0,1,1] neg_lo:[0,0,1] neg_hi:[0,0,1]
	v_pk_fma_f16 v149, v40, v33, v149 op_sel:[0,0,0] op_sel_hi:[0,1,1] neg_lo:[0,0,1] neg_hi:[0,0,1]
	v_pk_fma_f16 v150, v40, v34, v150 op_sel:[0,0,0] op_sel_hi:[0,1,1] neg_lo:[0,0,1] neg_hi:[0,0,1]
	v_pk_fma_f16 v151, v40, v35, v151 op_sel:[0,0,0] op_sel_hi:[0,1,1] neg_lo:[0,0,1] neg_hi:[0,0,1]
	ds_read_b128 v[96:99], v161 offset:4096
	ds_read_b128 v[100:103], v161 offset:5120
	ds_read_b128 v[104:107], v161 offset:6144
	ds_read_b128 v[108:111], v161 offset:7168
	s_add_u32 s17, s17, 1
	s_cmp_eq_u32 s17, 17
	s_cbranch_scc1 .Lk2_epi
	s_branch .Lk2_s00
